# shared attention code between layers + hand-scheduled MLA inner loop (early LDS writes, exps under PV MFMAs)
# speedup vs baseline: 1.0112x; 1.0112x over previous
; template <int DQK, bool FIXM> ...
;     ...
;     const int wid = tid >> 6, lane = tid & 63, r32 = lane & 31, hi = lane >> 5;
;     float m_reg = 0.f, l_reg = 0.f; f32x16 o0 = {}, o1 = {}, negm = {}; bf16x8 qr[NQ];
;     if (FIXM) { _Pragma("unroll") for (int r = 0; r < 16; ++r) negm[r] = -mfix; }
;     const bf16_t* Qw = Qp + (size_t)(wid * 32 + r32) * ldq + hi * 8;
; #pragma unroll
;     for (int d0 = 0; d0 < NQ; ++d0) qr[d0] = *(const bf16x8*)(Qw + d0 * 16);
;     if constexpr (DQK == 96) { if (qtok0 >= 0) {
;         const int t = qtok0 + wid * 32 + r32, gr = t >> 6, gc = t & 63;
; #pragma unroll
;         for (int e = 0; e < 2; ++e) { const f32x2* tp = (e == 0) ? rope + gr * 8 + hi * 4 : rope + 2048 + gc * 8 + hi * 4;
;             const f32x4 cs0 = *(const f32x4*)tp, cs1 = *(const f32x4*)(tp + 2);
;             const u32x4 w = __builtin_bit_cast(u32x4, qr[4 + e]); u32x4 o;
;             { const float x1 = bf16lo(w.x), x2 = bf16hi(w.x); o.x = cvt_pk_bf16(x1 * cs0[0] - x2 * cs0[1], x1 * cs0[1] + x2 * cs0[0]); }
;             { const float x1 = bf16lo(w.y), x2 = bf16hi(w.y); o.y = cvt_pk_bf16(x1 * cs0[2] - x2 * cs0[3], x1 * cs0[3] + x2 * cs0[2]); }
;             { const float x1 = bf16lo(w.z), x2 = bf16hi(w.z); o.z = cvt_pk_bf16(x1 * cs1[0] - x2 * cs1[1], x1 * cs1[1] + x2 * cs1[0]); }
; __device__ __forceinline__ void attn_phase(Frame& F, int li) {
;     ...
;     float mfixB; { float gq = 0.f, gk = 0.f; const float* a = F.in[15] + li * 64; const float* b = F.in[16] + li * 64;
;         for (int i = 0; i < 64; ++i) { gq = fmaxf(gq, fabsf(a[i])); gk = fmaxf(gk, fabsf(b[i])); } mfixB = 64.f * gq * gk * SC_B * 1.02f; }
;     constexpr int NU = 2048 + 32;
;     for (int u = F.vcu; u < NU; u += F.G) {
;         if (u < 1024 || (u >= 2048 && u < 2064)) {
;             const bool isctx = u >= 2048; const int uu = isctx ? u - 2048 : u;
;             const int b = isctx ? (uu >> 3) : (uu >> 9), h = isctx ? (uu & 7) : ((uu >> 6) & 7), qb = uu & 63;
;             const int q0 = isctx ? NLAT + b * CTXL : b * SEQ + qb * 256;
;             att::attn_unit<96, false>(QA + (size_t)q0 * 768 + h * 96, 768, KVA + h * 128, 1024, KR, KVA + h * 128 + 64, 1024, O + (size_t)q0 * 1024 + h * 64,
;                                b * SEQ, isctx ? 0 : 256, NLAT + b * CTXL, isctx ? 4 : 260, lds, F.tid, (const f32x2*)(F.ws + WS_ROPE), isctx ? -1 : qb * 256, 0.f);
.LBB0_486:
	s_add_u32 s4, s26, s2
	s_addc_u32 s5, s27, s3
	global_load_dwordx4 v[8:11], v1, s[4:5] offset:16
	global_load_dwordx4 v[12:15], v1, s[4:5]
	s_add_u32 s4, s36, s2
	s_addc_u32 s5, s37, s3
	global_load_dwordx4 v[16:19], v1, s[4:5]
	global_load_dwordx4 v[20:23], v1, s[4:5] offset:16
	s_add_u32 s2, s2, 32
	s_addc_u32 s3, s3, 0
	s_cmpk_eq_i32 s2, 0x100
	s_waitcnt vmcnt(0)
	v_max3_f32 v2, v5, |v12|, |v13|
	v_max3_f32 v2, v2, |v14|, |v15|
	v_max3_f32 v3, v6, |v16|, |v17|
	v_max3_f32 v2, v2, |v8|, |v9|
	v_max3_f32 v3, v3, |v18|, |v19|
	v_max3_f32 v5, v2, |v10|, |v11|
	v_max3_f32 v2, v3, |v20|, |v21|
	v_max3_f32 v6, v2, |v22|, |v23|
	s_cbranch_scc0 .LBB0_486
	s_mov_b32 s99, 0
.Latt_shared:
	s_cmpk_gt_i32 s14, 0x81f
	s_cbranch_scc1 .LBB0_548
	s_add_u32 s15, s0, 0x1ed00000
	s_addc_u32 s16, s1, 0
	s_add_u32 s17, s0, 0x17800000
	s_addc_u32 s18, s1, 0
	v_ashrrev_i32_e32 v1, 1, v4
	s_movk_i32 s2, 0xffe0
	s_add_u32 s19, s0, 0x20e00000
	v_bfi_b32 v186, s2, v1, v4
	v_ashrrev_i32_e32 v1, 3, v4
	s_addc_u32 s20, s1, 0
	s_movk_i32 s2, 0x600
	v_mov_b32_e32 v3, 0
	v_mad_i64_i32 v[196:197], s[2:3], v186, s2, 0
	v_and_b32_e32 v2, 32, v4
	s_add_u32 s21, s0, 0x1a900000
	v_lshrrev_b32_e32 v13, 1, v1
	v_lshl_add_u64 v[8:9], s[0:1], 0, v[2:3]
	s_mov_b64 s[2:3], 0x180000
	s_addc_u32 s22, s1, 0
	v_xor_b32_e32 v13, v13, v4
	v_and_b32_e32 v10, 63, v4
	v_ashrrev_i32_e32 v187, 31, v186
	v_lshlrev_b32_e32 v12, 3, v4
	v_lshl_add_u64 v[198:199], v[8:9], 0, s[2:3]
	s_add_u32 s23, s0, 0x21700000
	v_lshlrev_b32_e32 v2, 7, v1
	v_lshlrev_b32_e32 v13, 4, v13
	s_movk_i32 s2, 0x70
	v_lshlrev_b32_e32 v14, 4, v4
	v_lshlrev_b64 v[192:193], 10, v[186:187]
	v_lshlrev_b64 v[194:195], 11, v[186:187]
	s_addc_u32 s24, s1, 0
	v_and_or_b32 v187, v13, s2, v2
	v_lshrrev_b32_e32 v2, 5, v4
	v_bfe_u32 v13, v12, 5, 1
	s_mov_b32 s2, 0x7ffffe
	v_lshlrev_b32_e32 v10, 3, v10
	v_and_b32_e32 v15, 0xc0, v14
	v_lshlrev_b32_e32 v16, 1, v4
	v_and_b32_e32 v188, 56, v12
	s_add_u32 s25, s0, 0xec00000
	v_and_or_b32 v2, v2, s2, v13
	v_lshlrev_b32_e32 v13, 5, v1
	v_and_b32_e32 v12, 24, v12
	s_movk_i32 s2, 0xe0
	v_and_or_b32 v15, v10, 24, v15
	v_and_b32_e32 v16, 32, v16
	v_and_b32_e32 v10, 0x100, v10
	s_addc_u32 s26, s1, 0
	v_and_or_b32 v13, v13, s2, v12
	v_or3_b32 v10, v15, v16, v10
	s_add_i32 s2, 0, 0x3000
	v_lshlrev_b32_e32 v2, 9, v2
	v_add_u32_e32 v213, s2, v10
	s_mov_b64 s[2:3], 0x184000
	v_bfe_u32 v215, v4, 2, 6
	v_lshl_or_b32 v214, v13, 1, v2
	v_lshl_add_u64 v[202:203], v[8:9], 0, s[2:3]
	v_lshlrev_b32_e32 v2, 6, v215
	v_xor_b32_e32 v8, v14, v4
	v_and_or_b32 v216, v8, 48, v2
	v_lshlrev_b32_e32 v2, 1, v12
	v_bfe_u32 v11, v4, 5, 1
	v_lshl_add_u64 v[8:9], s[0:1], 0, v[2:3]
	v_bfe_u32 v2, v4, 2, 2
	v_lshrrev_b32_e32 v15, 1, v4
	v_bitop3_b32 v2, v11, v2, 2 bitop3:0x36
	v_bfe_u32 v16, v4, 1, 3
	v_bitop3_b32 v15, v11, v15, 7 bitop3:0x78
	v_lshlrev_b32_e32 v220, 4, v2
	v_mul_f32_e32 v2, 0x42800000, v5
	v_and_b32_e32 v7, 31, v4
	v_lshlrev_b32_e32 v209, 4, v15
	v_bitop3_b32 v15, v11, v16, 2 bitop3:0x36
	v_mul_f32_e32 v2, v6, v2
	s_movk_i32 s4, 0x100
	v_lshlrev_b32_e32 v201, 7, v7
	v_lshlrev_b32_e32 v210, 4, v15
	v_bitop3_b32 v15, v11, v16, 4 bitop3:0x36
	v_lshrrev_b32_e32 v10, 2, v4
	v_mul_f32_e32 v2, 0x3e38aa3b, v2
	v_add_u32_e32 v208, 0, v201
	v_lshlrev_b32_e32 v211, 4, v15
	v_bitop3_b32 v15, v11, v16, 6 bitop3:0x36
	v_cmp_gt_i32_e64 s[2:3], s4, v4
	s_mov_b64 s[0:1], 0x1ea00000
	v_lshlrev_b32_e32 v217, 6, v7
	v_bitop3_b32 v4, v11, v10, 3 bitop3:0x78
	v_mul_f32_e32 v18, 0xbf828f5c, v2
	v_lshlrev_b32_e32 v190, 2, v11
	v_add_u32_e32 v189, 0x80, v1
	v_lshlrev_b32_e32 v200, 3, v11
	v_add_u32_e32 v191, 64, v1
	s_mov_b32 s5, 0
	v_lshlrev_b32_e32 v212, 4, v15
	v_lshl_add_u64 v[204:205], v[8:9], 0, s[0:1]
	v_sub_u32_e32 v218, v208, v217
	v_lshlrev_b32_e32 v219, 4, v4
	v_mov_b32_e32 v19, v18
	v_mov_b32_e32 v20, v18
	v_mov_b32_e32 v21, v18
	v_mov_b32_e32 v22, v18
	v_mov_b32_e32 v23, v18
	v_mov_b32_e32 v24, v18
	v_mov_b32_e32 v25, v18
	v_mov_b32_e32 v26, v18
	v_mov_b32_e32 v27, v18
	v_mov_b32_e32 v28, v18
	v_mov_b32_e32 v29, v18
	v_mov_b32_e32 v30, v18
	v_mov_b32_e32 v31, v18
	v_mov_b32_e32 v32, v18
	v_mov_b32_e32 v33, v18
	v_add_u32_e32 v221, 0x100, v1
	v_or_b32_e32 v222, 0x100, v215
	s_movk_i32 s27, 0xfc00
	s_mov_b64 s[6:7], 0x400
	s_mov_b32 s28, 0x4138aa3b
	s_branch .LBB0_491

; #define LAS __attribute__((address_space(3)))
; __device__ __forceinline__ void finishSM(f32x16& p0, f32x16& p1, float alpha, float& l_reg, bf16x8& pa0, bf16x8& pa1, bf16x8& pa2, bf16x8& pa3) {
; #pragma unroll
;     for (int r = 0; r < 16; ++r) p1[r] = EXP_PROBE ? fmaf(p1[r], 0.001f, 1.f) : __builtin_amdgcn_exp2f(p1[r]);
;     float ps = 0.f;
; #pragma unroll
;     for (int r = 0; r < 16; ++r) ps += p0[r];
; #pragma unroll
;     for (int r = 0; r < 16; ++r) ps += p1[r];
;     { auto rr = __builtin_amdgcn_permlane32_swap(__float_as_uint(ps), __float_as_uint(ps), false, false);
;       ps = __uint_as_float(rr[0]) + __uint_as_float(rr[1]); }
;     l_reg = l_reg * alpha + ps;
;     ATT_PKN(p0, 0, pa0); ATT_PKN(p0, 8, pa1); ATT_PKN(p1, 0, pa2); ATT_PKN(p1, 8, pa3);
; }
; template <int DQK> __device__ __forceinline__ void qkt(f32x16& p0, f32x16& p1, const LAS char* buf, const bf16x8* qr, int r32, int hi, const f32x16& negm) {
; #pragma unroll
;     for (int d0 = 0; d0 < 4; ++d0) { const int ch = d0 * 2 + hi;
;         const bf16x8 b0 = *(const LAS bf16x8*)(buf + B_KN + swz64(r32, ch));
;         const bf16x8 b1 = *(const LAS bf16x8*)(buf + B_KN + swz64(32 + r32, ch));
;         p0 = __builtin_amdgcn_mfma_f32_32x32x16_bf16(b0, qr[d0], d0 == 0 ? negm : p0, 0, 0, 0);
;         p1 = __builtin_amdgcn_mfma_f32_32x32x16_bf16(b1, qr[d0], d0 == 0 ? negm : p1, 0, 0, 0); }
;     if constexpr (DQK == 96) {
; #pragma unroll
;         for (int d0 = 0; d0 < 2; ++d0) { const int ch = d0 * 2 + hi;
;             const bf16x8 b0 = *(const LAS bf16x8*)(buf + B_KR + swz32(r32, ch));
;             const bf16x8 b1 = *(const LAS bf16x8*)(buf + B_KR + swz32(32 + r32, ch));
;             p0 = __builtin_amdgcn_mfma_f32_32x32x16_bf16(b0, qr[4 + d0], p0, 0, 0, 0);
;             p1 = __builtin_amdgcn_mfma_f32_32x32x16_bf16(b1, qr[4 + d0], p1, 0, 0, 0); }
;     }
; }
; template <int DQK, bool FIXM> ...
;     ...
;         if (!NOBAR_PROBE) __syncthreads();
;         SBAR(); qkt<DQK>(pB0, pB1, lds + bK, qr, r32, hi, negm);
;         finishSM(pA0, pA1, alA, l_reg, pa0, pa1, pa2, pa3); SBAR();
;         SLOAD(1, j + 2); SBAR();
;         if constexpr (FIXM) pv_psm<true>(o0, o1, vb0 + bV, pa0, pa1, pa2, pa3, pB0, pB1, m_reg, negm, alB); else { PVO(bV); partialSM<false>(pB0, pB1, m_reg, negm, alB); }
;         SWAIT(); SWRITEO(bW, 0);
;         if (!FIXM) RESC(alB); ROT();
.LBB0_523:
	s_mov_b32 s10, s0
	s_waitcnt lgkmcnt(0)
	s_barrier
	v_add_u32_e32 v2, s13, v201
	v_add_u32_e32 v8, v2, v209
	ds_read_b128 v[4:7], v8
	ds_read_b128 v[8:11], v8 offset:4096
	v_add_u32_e32 v246, v2, v210
	ds_read_b128 v[174:177], v246
	ds_read_b128 v[246:249], v246 offset:4096
	v_add_u32_e32 v78, v2, v211
	ds_read_b128 v[250:253], v78
	ds_read_b128 v[78:81], v78 offset:4096
	v_add_u32_e32 v16, v2, v212
	ds_read_b128 v[12:15], v16
	v_add_u32_e32 v2, s13, v217
	v_exp_f32_e32 v98, v98
	v_exp_f32_e32 v99, v99
	v_exp_f32_e32 v100, v100
	v_exp_f32_e32 v101, v101
	v_exp_f32_e32 v102, v102
	v_exp_f32_e32 v103, v103
	v_exp_f32_e32 v104, v104
	v_exp_f32_e32 v105, v105
	s_waitcnt lgkmcnt(6)
	v_mfma_f32_32x32x16_bf16 v[130:145], v[4:7], v[166:169], v[82:97]
	ds_read_b128 v[4:7], v16 offset:4096
	v_exp_f32_e32 v106, v106
	v_exp_f32_e32 v107, v107
	v_exp_f32_e32 v108, v108
	s_waitcnt lgkmcnt(6)
	v_mfma_f32_32x32x16_bf16 v[114:129], v[8:11], v[166:169], v[82:97]
	v_add_u32_e32 v16, v2, v219
	ds_read_b128 v[8:11], v16 offset:8192
	v_exp_f32_e32 v109, v109
	v_exp_f32_e32 v110, v110
	v_exp_f32_e32 v111, v111
	s_waitcnt lgkmcnt(6)
	v_mfma_f32_32x32x16_bf16 v[130:145], v[174:177], v[162:165], v[130:145]
	ds_read_b128 v[174:177], v16 offset:10240
	v_exp_f32_e32 v112, v112
	v_exp_f32_e32 v113, v113
	v_add_f32_e32 v17, 0, v243
	v_add_f32_e32 v17, v245, v17
	s_waitcnt lgkmcnt(6)
	v_mfma_f32_32x32x16_bf16 v[114:129], v[246:249], v[162:165], v[114:129]
	v_add_u32_e32 v16, v2, v220
	ds_read_b128 v[246:249], v16 offset:8192
	v_add_f32_e32 v17, v241, v17
	v_add_f32_e32 v17, v244, v17
	v_add_f32_e32 v17, v239, v17
	v_add_f32_e32 v17, v242, v17
	v_add_f32_e32 v17, v238, v17
	s_waitcnt lgkmcnt(6)
	v_mfma_f32_32x32x16_bf16 v[130:145], v[250:253], v[158:161], v[130:145]
	ds_read_b128 v[250:253], v16 offset:10240
	v_add_f32_e32 v17, v240, v17
	v_add_f32_e32 v17, v236, v17
	v_add_f32_e32 v17, v237, v17
	v_add_f32_e32 v17, v233, v17
	v_add_f32_e32 v17, v235, v17
	v_add_f32_e32 v17, v231, v17
	s_waitcnt lgkmcnt(6)
	v_mfma_f32_32x32x16_bf16 v[114:129], v[78:81], v[158:161], v[114:129]
	v_add_f32_e32 v17, v234, v17
	v_add_f32_e32 v17, v230, v17
	v_add_f32_e32 v17, v232, v17
	v_add_f32_e32 v17, v98, v17
	v_add_f32_e32 v17, v99, v17
	v_add_f32_e32 v17, v100, v17
	s_waitcnt lgkmcnt(5)
	v_mfma_f32_32x32x16_bf16 v[130:145], v[12:15], v[154:157], v[130:145]
	v_add_f32_e32 v17, v101, v17
	v_add_f32_e32 v17, v102, v17
	v_add_f32_e32 v17, v103, v17
	v_add_f32_e32 v17, v104, v17
	v_add_f32_e32 v17, v105, v17
	v_add_f32_e32 v17, v106, v17
	s_waitcnt lgkmcnt(4)
	v_mfma_f32_32x32x16_bf16 v[114:129], v[4:7], v[154:157], v[114:129]
	v_add_f32_e32 v17, v107, v17
	v_add_f32_e32 v17, v108, v17
	v_add_f32_e32 v17, v109, v17
	v_add_f32_e32 v17, v110, v17
	v_add_f32_e32 v17, v111, v17
	v_add_f32_e32 v17, v112, v17
	s_waitcnt lgkmcnt(3)
	v_mfma_f32_32x32x16_bf16 v[130:145], v[8:11], v[150:153], v[130:145]
	v_add_f32_e32 v228, v113, v17
	v_mov_b32_e32 v229, v228
	v_cvt_pk_bf16_f32 v74, v243, v245
	v_cvt_pk_bf16_f32 v75, v241, v244
	v_cvt_pk_bf16_f32 v76, v239, v242
	v_cvt_pk_bf16_f32 v77, v238, v240
	v_permlane32_swap_b32_e32 v228, v229
	s_waitcnt lgkmcnt(2)
	v_mfma_f32_32x32x16_bf16 v[114:129], v[174:177], v[150:153], v[114:129]
	v_cvt_pk_bf16_f32 v66, v236, v237
	v_cvt_pk_bf16_f32 v67, v233, v235
	v_cvt_pk_bf16_f32 v68, v231, v234
	v_cvt_pk_bf16_f32 v69, v230, v232
	v_cvt_pk_bf16_f32 v70, v98, v99
	s_waitcnt lgkmcnt(1)
	v_mfma_f32_32x32x16_bf16 v[130:145], v[246:249], v[146:149], v[130:145]
	v_cvt_pk_bf16_f32 v71, v100, v101
	v_cvt_pk_bf16_f32 v72, v102, v103
	v_cvt_pk_bf16_f32 v73, v104, v105
	v_cvt_pk_bf16_f32 v12, v106, v107
	v_cvt_pk_bf16_f32 v13, v108, v109
	s_waitcnt lgkmcnt(0)
	v_mfma_f32_32x32x16_bf16 v[114:129], v[250:253], v[146:149], v[114:129]
	v_cvt_pk_bf16_f32 v14, v110, v111
	v_cvt_pk_bf16_f32 v15, v112, v113
	s_add_i32 s36, s35, -1
	s_cmp_lt_u32 s36, s30
	s_cselect_b32 s0, 0, s30
	s_cselect_b32 s1, s29, s34
	s_lshl_b32 s0, s0, 6
	s_sub_i32 s37, s1, s0
	v_add_u32_e32 v2, s37, v225
	v_subrev_u32_e32 v4, 64, v2
	v_ashrrev_i32_e32 v5, 31, v4
	v_lshlrev_b64 v[4:5], 11, v[4:5]
	v_lshl_add_u64 v[4:5], v[206:207], 0, v[4:5]
	global_load_dwordx4 v[8:11], v[4:5], off
	s_nop 0
	global_load_dwordx4 v[4:7], v[4:5], off offset:128
	v_add_u32_e32 v2, s37, v226
	v_subrev_u32_e32 v16, 64, v2
	v_ashrrev_i32_e32 v17, 31, v16
	v_lshlrev_b64 v[16:17], 6, v[16:17]
	v_lshl_add_u64 v[16:17], v[204:205], 0, v[16:17]
	global_load_dwordx4 v[174:177], v[16:17], off
	v_add_u32_e32 v17, s11, v213
	ds_read_b64_tr_b16 v[78:79], v17 offset:0
	ds_read_b64_tr_b16 v[80:81], v17 offset:1024
	ds_read_b64_tr_b16 v[98:99], v17 offset:2048
	ds_read_b64_tr_b16 v[100:101], v17 offset:3072
	ds_read_b64_tr_b16 v[102:103], v17 offset:4096
	ds_read_b64_tr_b16 v[104:105], v17 offset:5120
	ds_read_b64_tr_b16 v[106:107], v17 offset:6144
	ds_read_b64_tr_b16 v[108:109], v17 offset:7168
	v_max_f32_e32 v2, v131, v131
	v_max_f32_e32 v16, v130, v130
	v_max_f32_e32 v2, v16, v2
	v_max3_f32 v2, v2, v132, v133
	v_max3_f32 v2, v2, v134, v135
	v_max3_f32 v2, v2, v136, v137
	v_max3_f32 v2, v2, v138, v139
	v_max3_f32 v2, v2, v140, v141
	v_max3_f32 v2, v2, v142, v143
	s_waitcnt lgkmcnt(0)
	v_mfma_f32_32x32x16_bf16 v[50:65], v[78:81], v[74:77], v[50:65]
	ds_read_b64_tr_b16 v[78:79], v17 offset:512
	ds_read_b64_tr_b16 v[80:81], v17 offset:1536
	v_max3_f32 v2, v2, v144, v145
	v_max3_f32 v2, v2, v114, v115
	v_max3_f32 v2, v2, v116, v117
	v_mfma_f32_32x32x16_bf16 v[50:65], v[98:101], v[66:69], v[50:65]
	ds_read_b64_tr_b16 v[98:99], v17 offset:2560
	ds_read_b64_tr_b16 v[100:101], v17 offset:3584
	v_max3_f32 v2, v2, v118, v119
	v_max3_f32 v2, v2, v120, v121
	v_max3_f32 v2, v2, v122, v123
	v_mfma_f32_32x32x16_bf16 v[50:65], v[102:105], v[70:73], v[50:65]
	ds_read_b64_tr_b16 v[102:103], v17 offset:4608
	ds_read_b64_tr_b16 v[104:105], v17 offset:5632
	ds_read_b64_tr_b16 v[110:111], v17 offset:6656
	ds_read_b64_tr_b16 v[112:113], v17 offset:7680
	v_max3_f32 v2, v2, v124, v125
	v_max3_f32 v2, v2, v126, v127
	v_max3_f32 v2, v2, v128, v129
	v_mfma_f32_32x32x16_bf16 v[50:65], v[106:109], v[12:15], v[50:65]
	v_mov_b32_e32 v16, v2
	s_nop 1
	v_permlane32_swap_b32_e32 v2, v16
	v_max_f32_e32 v16, v16, v16
	v_max_f32_e32 v2, v2, v2
	v_max_f32_e32 v2, v2, v16
	v_cmp_ge_f32_e32 vcc, s28, v2
	s_cmp_eq_u64 vcc, exec
	s_cbranch_scc0 .LBB0_542
	v_mov_b32_e32 v2, 1.0
; __device__ __forceinline__ void finishSM(f32x16& p0, f32x16& p1, float alpha, float& l_reg, bf16x8& pa0, bf16x8& pa1, bf16x8& pa2, bf16x8& pa3) {
; #pragma unroll
;     for (int r = 0; r < 16; ++r) p1[r] = EXP_PROBE ? fmaf(p1[r], 0.001f, 1.f) : __builtin_amdgcn_exp2f(p1[r]);
;     float ps = 0.f;
; #pragma unroll
;     for (int r = 0; r < 16; ++r) ps += p0[r];
; #pragma unroll
;     for (int r = 0; r < 16; ++r) ps += p1[r];
;     { auto rr = __builtin_amdgcn_permlane32_swap(__float_as_uint(ps), __float_as_uint(ps), false, false);
;       ps = __uint_as_float(rr[0]) + __uint_as_float(rr[1]); }
;     l_reg = l_reg * alpha + ps;
;     ATT_PKN(p0, 0, pa0); ATT_PKN(p0, 8, pa1); ATT_PKN(p1, 0, pa2); ATT_PKN(p1, 8, pa3);
; }
; template <int DQK> __device__ __forceinline__ void qkt(f32x16& p0, f32x16& p1, const LAS char* buf, const bf16x8* qr, int r32, int hi, const f32x16& negm) {
; #pragma unroll
;     for (int d0 = 0; d0 < 4; ++d0) { const int ch = d0 * 2 + hi;
;         const bf16x8 b0 = *(const LAS bf16x8*)(buf + B_KN + swz64(r32, ch));
;         const bf16x8 b1 = *(const LAS bf16x8*)(buf + B_KN + swz64(32 + r32, ch));
;         p0 = __builtin_amdgcn_mfma_f32_32x32x16_bf16(b0, qr[d0], d0 == 0 ? negm : p0, 0, 0, 0);
;         p1 = __builtin_amdgcn_mfma_f32_32x32x16_bf16(b1, qr[d0], d0 == 0 ? negm : p1, 0, 0, 0); }
;     if constexpr (DQK == 96) {
; #pragma unroll
;         for (int d0 = 0; d0 < 2; ++d0) { const int ch = d0 * 2 + hi;
;             const bf16x8 b0 = *(const LAS bf16x8*)(buf + B_KR + swz32(r32, ch));
;             const bf16x8 b1 = *(const LAS bf16x8*)(buf + B_KR + swz32(32 + r32, ch));
; template <int DQK, bool FIXM> ...
;     ...
;         if constexpr (FIXM) pv_psm<true>(o0, o1, vb0 + bV, pa0, pa1, pa2, pa3, pB0, pB1, m_reg, negm, alB); else { PVO(bV); partialSM<false>(pB0, pB1, m_reg, negm, alB); }
;         SWAIT(); SWRITEO(bW, 0);
;         if (!FIXM) RESC(alB); ROT();
;         if (!NOBAR_PROBE) __syncthreads();
;         SBAR(); qkt<DQK>(pA0, pA1, lds + bK, qr, r32, hi, negm);
;         finishSM(pB0, pB1, alB, l_reg, pa0, pa1, pa2, pa3); SBAR();
;         if (j + 3 < NT) SLOAD(0, j + 3); SBAR();
;         if constexpr (FIXM) pv_psm<true>(o0, o1, vb0 + bV, pa0, pa1, pa2, pa3, pA0, pA1, m_reg, negm, alA); else { PVO(bV); partialSM<false>(pA0, pA1, m_reg, negm, alA); }
;         SWAIT(); SWRITEO(bW, 1);
;         if (!FIXM) RESC(alA); ROT();
.LBB0_527:
	s_waitcnt lgkmcnt(0)
	v_mfma_f32_32x32x16_bf16 v[34:49], v[78:81], v[74:77], v[34:49]
	s_waitcnt vmcnt(3)
	v_add_u32_e32 v17, s10, v187
	ds_write_b128 v17, v[178:181]
	v_add_u32_e32 v17, s10, v214
	ds_write_b128 v17, v[182:185] offset:12288
	s_and_saveexec_b64 s[0:1], s[2:3]
	v_add_u32_e32 v17, s10, v216
	ds_write_b128 v17, v[170:173] offset:8192
	s_or_b64 exec, exec, s[0:1]
	v_exp_f32_e32 v16, v130
	v_exp_f32_e32 v234, v131
	v_mfma_f32_32x32x16_bf16 v[34:49], v[98:101], v[66:69], v[34:49]
	v_exp_f32_e32 v235, v132
	v_exp_f32_e32 v236, v133
	v_exp_f32_e32 v237, v134
	v_exp_f32_e32 v238, v135
	v_mfma_f32_32x32x16_bf16 v[34:49], v[102:105], v[70:73], v[34:49]
	v_exp_f32_e32 v239, v136
	v_exp_f32_e32 v240, v137
	v_exp_f32_e32 v241, v138
	v_exp_f32_e32 v242, v139
	v_exp_f32_e32 v243, v140
	v_mfma_f32_32x32x16_bf16 v[34:49], v[110:113], v[12:15], v[34:49]
	v_exp_f32_e32 v244, v141
	v_exp_f32_e32 v245, v142
	v_exp_f32_e32 v246, v143
	v_exp_f32_e32 v247, v144
	v_exp_f32_e32 v248, v145
	v_cmp_gt_f32_e32 vcc, 1.0, v2
	s_cbranch_vccz .LBB0_531
	s_nop 7
	s_nop 7
	v_pk_mul_f32 v[64:65], v[64:65], v[2:3] op_sel_hi:[1,0]
	v_pk_mul_f32 v[62:63], v[62:63], v[2:3] op_sel_hi:[1,0]
	v_pk_mul_f32 v[60:61], v[60:61], v[2:3] op_sel_hi:[1,0]
	v_pk_mul_f32 v[58:59], v[58:59], v[2:3] op_sel_hi:[1,0]
	v_pk_mul_f32 v[56:57], v[56:57], v[2:3] op_sel_hi:[1,0]
	v_pk_mul_f32 v[54:55], v[54:55], v[2:3] op_sel_hi:[1,0]
	v_pk_mul_f32 v[52:53], v[52:53], v[2:3] op_sel_hi:[1,0]
	v_pk_mul_f32 v[50:51], v[50:51], v[2:3] op_sel_hi:[1,0]
	v_pk_mul_f32 v[48:49], v[48:49], v[2:3] op_sel_hi:[1,0]
	v_pk_mul_f32 v[46:47], v[46:47], v[2:3] op_sel_hi:[1,0]
	v_pk_mul_f32 v[44:45], v[44:45], v[2:3] op_sel_hi:[1,0]
	v_pk_mul_f32 v[42:43], v[42:43], v[2:3] op_sel_hi:[1,0]
	v_pk_mul_f32 v[40:41], v[40:41], v[2:3] op_sel_hi:[1,0]
	v_pk_mul_f32 v[38:39], v[38:39], v[2:3] op_sel_hi:[1,0]
	v_pk_mul_f32 v[36:37], v[36:37], v[2:3] op_sel_hi:[1,0]
	v_pk_mul_f32 v[34:35], v[34:35], v[2:3] op_sel_hi:[1,0]
.LBB0_531:
	s_waitcnt lgkmcnt(0)
	s_barrier
	v_add_u32_e32 v17, s10, v201
	v_add_u32_e32 v70, v17, v209
	ds_read_b128 v[66:69], v70
	ds_read_b128 v[70:73], v70 offset:4096
	v_add_u32_e32 v78, v17, v210
	ds_read_b128 v[74:77], v78
	ds_read_b128 v[78:81], v78 offset:4096
	v_add_u32_e32 v182, v17, v211
	ds_read_b128 v[178:181], v182
	ds_read_b128 v[182:185], v182 offset:4096
	v_add_u32_e32 v253, v17, v212
	ds_read_b128 v[170:173], v253
	v_add_u32_e32 v17, s10, v217
	v_exp_f32_e32 v250, v125
	v_exp_f32_e32 v251, v126
	v_exp_f32_e32 v252, v127
	v_exp_f32_e32 v128, v128
	v_exp_f32_e32 v129, v129
	v_exp_f32_e32 v249, v124
	v_exp_f32_e32 v12, v114
	v_exp_f32_e32 v13, v115
	s_waitcnt lgkmcnt(6)
	v_mfma_f32_32x32x16_bf16 v[130:145], v[66:69], v[166:169], v[82:97]
	ds_read_b128 v[66:69], v253 offset:4096
	v_exp_f32_e32 v14, v116
	v_exp_f32_e32 v15, v117
	v_exp_f32_e32 v116, v118
	s_waitcnt lgkmcnt(6)
	v_mfma_f32_32x32x16_bf16 v[98:113], v[70:73], v[166:169], v[82:97]
	v_add_u32_e32 v253, v17, v219
	ds_read_b128 v[70:73], v253 offset:8192
	v_exp_f32_e32 v117, v119
	v_exp_f32_e32 v230, v120
	v_exp_f32_e32 v231, v121
	s_waitcnt lgkmcnt(6)
	v_mfma_f32_32x32x16_bf16 v[130:145], v[74:77], v[162:165], v[130:145]
	ds_read_b128 v[74:77], v253 offset:10240
	v_exp_f32_e32 v232, v122
	v_exp_f32_e32 v233, v123
	v_add_f32_e32 v114, 0, v16
	v_add_f32_e32 v114, v234, v114
	s_waitcnt lgkmcnt(6)
	v_mfma_f32_32x32x16_bf16 v[98:113], v[78:81], v[162:165], v[98:113]
	v_add_u32_e32 v253, v17, v220
	ds_read_b128 v[78:81], v253 offset:8192
	v_add_f32_e32 v114, v235, v114
	v_add_f32_e32 v114, v236, v114
	v_add_f32_e32 v114, v237, v114
	v_add_f32_e32 v114, v238, v114
	v_add_f32_e32 v114, v239, v114
	s_waitcnt lgkmcnt(6)
	v_mfma_f32_32x32x16_bf16 v[130:145], v[178:181], v[158:161], v[130:145]
	ds_read_b128 v[178:181], v253 offset:10240
	v_add_f32_e32 v114, v240, v114
	v_add_f32_e32 v114, v241, v114
	v_add_f32_e32 v114, v242, v114
	v_add_f32_e32 v114, v243, v114
	v_add_f32_e32 v114, v244, v114
	v_add_f32_e32 v114, v245, v114
	s_waitcnt lgkmcnt(6)
	v_mfma_f32_32x32x16_bf16 v[98:113], v[182:185], v[158:161], v[98:113]
	v_add_f32_e32 v114, v246, v114
	v_add_f32_e32 v114, v247, v114
	v_add_f32_e32 v114, v248, v114
	v_add_f32_e32 v114, v12, v114
	v_add_f32_e32 v114, v13, v114
	v_add_f32_e32 v114, v14, v114
	s_waitcnt lgkmcnt(5)
	v_mfma_f32_32x32x16_bf16 v[130:145], v[170:173], v[154:157], v[130:145]
	v_add_f32_e32 v114, v15, v114
	v_add_f32_e32 v114, v116, v114
	v_add_f32_e32 v114, v117, v114
	v_add_f32_e32 v114, v230, v114
	v_add_f32_e32 v114, v231, v114
	v_add_f32_e32 v114, v232, v114
	s_waitcnt lgkmcnt(4)
	v_mfma_f32_32x32x16_bf16 v[98:113], v[66:69], v[154:157], v[98:113]
	v_add_f32_e32 v114, v233, v114
	v_add_f32_e32 v114, v249, v114
	v_add_f32_e32 v114, v250, v114
	v_add_f32_e32 v114, v251, v114
	v_add_f32_e32 v114, v252, v114
	v_add_f32_e32 v114, v128, v114
	s_waitcnt lgkmcnt(3)
	v_mfma_f32_32x32x16_bf16 v[130:145], v[70:73], v[150:153], v[130:145]
	v_add_f32_e32 v126, v129, v114
	v_mov_b32_e32 v127, v126
	v_cvt_pk_bf16_f32 v122, v16, v234
	v_cvt_pk_bf16_f32 v123, v235, v236
	v_cvt_pk_bf16_f32 v124, v237, v238
	v_cvt_pk_bf16_f32 v125, v239, v240
	v_permlane32_swap_b32_e32 v126, v127
	s_waitcnt lgkmcnt(2)
	v_mfma_f32_32x32x16_bf16 v[98:113], v[74:77], v[150:153], v[98:113]
	v_cvt_pk_bf16_f32 v118, v241, v242
	v_cvt_pk_bf16_f32 v119, v243, v244
	v_cvt_pk_bf16_f32 v120, v245, v246
	v_cvt_pk_bf16_f32 v121, v247, v248
	v_cvt_pk_bf16_f32 v114, v12, v13
	s_waitcnt lgkmcnt(1)
	v_mfma_f32_32x32x16_bf16 v[130:145], v[78:81], v[146:149], v[130:145]
	v_cvt_pk_bf16_f32 v115, v14, v15
	v_cvt_pk_bf16_f32 v116, v116, v117
	v_cvt_pk_bf16_f32 v117, v230, v231
	v_cvt_pk_bf16_f32 v12, v232, v233
	v_cvt_pk_bf16_f32 v13, v249, v250
	s_waitcnt lgkmcnt(0)
	v_mfma_f32_32x32x16_bf16 v[98:113], v[178:181], v[146:149], v[98:113]
	v_cvt_pk_bf16_f32 v14, v251, v252
	v_cvt_pk_bf16_f32 v15, v128, v129
	s_cmp_ge_u32 s35, s31
	s_cbranch_scc1 .Lmla_b_noload
	s_cmp_lt_u32 s35, s30
	s_cselect_b32 s0, 0, s30
	s_cselect_b32 s1, s29, s34
	s_lshl_b32 s0, s0, 6
	s_sub_i32 s37, s1, s0
	v_add_u32_e32 v128, s37, v225
	v_ashrrev_i32_e32 v129, 31, v128
	v_lshlrev_b64 v[128:129], 11, v[128:129]
	v_lshl_add_u64 v[128:129], v[206:207], 0, v[128:129]
	global_load_dwordx4 v[178:181], v[128:129], off
	global_load_dwordx4 v[182:185], v[128:129], off offset:128
	v_add_u32_e32 v128, s37, v226
	v_ashrrev_i32_e32 v129, 31, v128
	v_lshlrev_b64 v[128:129], 6, v[128:129]
	v_lshl_add_u64 v[128:129], v[204:205], 0, v[128:129]
	global_load_dwordx4 v[170:173], v[128:129], off
; #define SWRITEO(boff, i) do { *(LAS bf16x8*)(lds + (boff) + kn_st) = skn[i]; *(LAS bf16x8*)(lds + (boff) + v_stw) = sv[i]; if (krw) *(LAS bf16x8*)(lds + (boff) + kr_st) = skr[i]; } while (0)
; #define PVO(boff) do { pv_one<0>(o0, vb0 + (boff), pa0, pa1, pa2, pa3); pv_one<1>(o1, vb0 + (boff), pa0, pa1, pa2, pa3); } while (0)
; #define SWAIT() asm volatile("s_waitcnt vmcnt(2)" ::: "memory")
; #define RESC(a) do { if (__any((a) < 1.f)) { _Pragma("unroll") for (int r = 0; r < 16; ++r) { o0[r] *= (a); o1[r] *= (a); } } } while (0)
; #define ROT() do { const int _t = bV; bV = bK; bK = bW; bW = _t; } while (0)
; __device__ __forceinline__ float psm_max(const f32x16& p0, const f32x16& p1) {
;     float pmax = p0[0];
; #pragma unroll
;     for (int r = 1; r < 16; ++r) pmax = fmaxf(pmax, p0[r]);
; #pragma unroll
;     for (int r = 0; r < 16; ++r) pmax = fmaxf(pmax, p1[r]);
;     { auto rr = __builtin_amdgcn_permlane32_swap(__float_as_uint(pmax), __float_as_uint(pmax), false, false);
;       pmax = fmaxf(__uint_as_float(rr[0]), __uint_as_float(rr[1])); }
;     return pmax;
; }
; template <bool FIRST> __device__ __forceinline__ void psm_apply(f32x16& p0, f32x16& p1, float pmax, float& m_reg, f32x16& negm, float& alpha) {
;     alpha = 1.f;
;     if (FIRST || !__builtin_expect(__all(pmax <= THR2), 1)) {
;         const float delta = FIRST ? pmax : fmaxf(pmax, 0.f);
;         if (!FIRST) alpha = __builtin_amdgcn_exp2f(-delta);
;         m_reg += delta;
; #pragma unroll
;         for (int r = 0; r < 16; ++r) { p0[r] -= delta; p1[r] -= delta; negm[r] = -m_reg; }
;     }
; #pragma unroll
;     for (int r = 0; r < 16; ++r) p0[r] = EXP_PROBE ? fmaf(p0[r], 0.001f, 1.f) : __builtin_amdgcn_exp2f(p0[r]);
; }
; template <bool FIRST> __device__ __forceinline__ void partialSM(f32x16& p0, f32x16& p1, float& m_reg, f32x16& negm, float& alpha) {
;     const float pmax = psm_max(p0, p1); psm_apply<FIRST>(p0, p1, pmax, m_reg, negm, alpha);
; }
; template <int DQK, bool FIXM> ...
;     ...
;         if constexpr (FIXM) pv_psm<true>(o0, o1, vb0 + bV, pa0, pa1, pa2, pa3, pA0, pA1, m_reg, negm, alA); else { PVO(bV); partialSM<false>(pA0, pA1, m_reg, negm, alA); }
;         SWAIT(); SWRITEO(bW, 1);
;         if (!FIXM) RESC(alA); ROT();
.Lmla_b_ld_done:
	v_add_u32_e32 v16, s13, v213
	ds_read_b64_tr_b16 v[230:231], v16 offset:0
	ds_read_b64_tr_b16 v[232:233], v16 offset:1024
	ds_read_b64_tr_b16 v[234:235], v16 offset:2048
	ds_read_b64_tr_b16 v[236:237], v16 offset:3072
	ds_read_b64_tr_b16 v[238:239], v16 offset:4096
	ds_read_b64_tr_b16 v[240:241], v16 offset:5120
	ds_read_b64_tr_b16 v[242:243], v16 offset:6144
	ds_read_b64_tr_b16 v[244:245], v16 offset:7168
	v_max_f32_e32 v129, v131, v131
	v_max_f32_e32 v128, v130, v130
	v_max_f32_e32 v128, v128, v129
	v_max3_f32 v128, v128, v132, v133
	v_max3_f32 v128, v128, v134, v135
	v_max3_f32 v128, v128, v136, v137
	v_max3_f32 v128, v128, v138, v139
	v_max3_f32 v128, v128, v140, v141
	v_max3_f32 v128, v128, v142, v143
	s_waitcnt lgkmcnt(0)
	v_mfma_f32_32x32x16_bf16 v[50:65], v[230:233], v[122:125], v[50:65]
	ds_read_b64_tr_b16 v[230:231], v16 offset:512
	ds_read_b64_tr_b16 v[232:233], v16 offset:1536
	v_max3_f32 v128, v128, v144, v145
	v_max3_f32 v128, v128, v98, v99
	v_max3_f32 v128, v128, v100, v101
	v_mfma_f32_32x32x16_bf16 v[50:65], v[234:237], v[118:121], v[50:65]
	ds_read_b64_tr_b16 v[234:235], v16 offset:2560
	ds_read_b64_tr_b16 v[236:237], v16 offset:3584
	v_max3_f32 v128, v128, v102, v103
	v_max3_f32 v128, v128, v104, v105
	v_max3_f32 v128, v128, v106, v107
	v_mfma_f32_32x32x16_bf16 v[50:65], v[238:241], v[114:117], v[50:65]
	ds_read_b64_tr_b16 v[238:239], v16 offset:4608
	ds_read_b64_tr_b16 v[240:241], v16 offset:5632
	ds_read_b64_tr_b16 v[246:247], v16 offset:6656
	ds_read_b64_tr_b16 v[248:249], v16 offset:7680
	v_max3_f32 v128, v128, v108, v109
	v_max3_f32 v128, v128, v110, v111
	v_max3_f32 v128, v128, v112, v113
	v_mfma_f32_32x32x16_bf16 v[50:65], v[242:245], v[12:15], v[50:65]
	v_mov_b32_e32 v129, v128
	s_nop 1
	v_permlane32_swap_b32_e32 v128, v129
	v_max_f32_e32 v129, v129, v129
	v_max_f32_e32 v128, v128, v128
	v_max_f32_e32 v128, v128, v129
	v_cmp_ge_f32_e32 vcc, s28, v128
	s_cmp_eq_u64 vcc, exec
	v_mov_b32_e32 v16, 1.0
	s_cbranch_scc0 .LBB0_543
.LBB0_536:
	s_waitcnt lgkmcnt(0)
	v_mfma_f32_32x32x16_bf16 v[34:49], v[230:233], v[122:125], v[34:49]
	s_waitcnt vmcnt(3)
	v_add_u32_e32 v129, s11, v187
	ds_write_b128 v129, v[8:11]
	v_add_u32_e32 v129, s11, v214
	ds_write_b128 v129, v[4:7] offset:12288
	s_and_saveexec_b64 s[0:1], s[2:3]
	v_add_u32_e32 v129, s11, v216
	ds_write_b128 v129, v[174:177] offset:8192
	s_or_b64 exec, exec, s[0:1]
	v_exp_f32_e32 v243, v130
	v_exp_f32_e32 v245, v131
	v_mfma_f32_32x32x16_bf16 v[34:49], v[234:237], v[118:121], v[34:49]
	v_exp_f32_e32 v244, v133
	v_exp_f32_e32 v242, v135
	v_exp_f32_e32 v233, v140
	v_exp_f32_e32 v231, v142
	v_mfma_f32_32x32x16_bf16 v[34:49], v[238:241], v[114:117], v[34:49]
	v_exp_f32_e32 v230, v144
	v_exp_f32_e32 v232, v145
	v_exp_f32_e32 v236, v138
	v_exp_f32_e32 v237, v139
	v_exp_f32_e32 v235, v141
	v_mfma_f32_32x32x16_bf16 v[34:49], v[246:249], v[12:15], v[34:49]
	v_exp_f32_e32 v234, v143
	v_exp_f32_e32 v241, v132
	v_exp_f32_e32 v239, v134
	v_exp_f32_e32 v238, v136
	v_exp_f32_e32 v240, v137
	v_cmp_gt_f32_e32 vcc, 1.0, v16
	s_cbranch_vccz .LBB0_540
	s_nop 7
	s_nop 7
	v_pk_mul_f32 v[64:65], v[64:65], v[16:17] op_sel_hi:[1,0]
	v_pk_mul_f32 v[62:63], v[62:63], v[16:17] op_sel_hi:[1,0]
	v_pk_mul_f32 v[60:61], v[60:61], v[16:17] op_sel_hi:[1,0]
	v_pk_mul_f32 v[58:59], v[58:59], v[16:17] op_sel_hi:[1,0]
	v_pk_mul_f32 v[56:57], v[56:57], v[16:17] op_sel_hi:[1,0]
	v_pk_mul_f32 v[54:55], v[54:55], v[16:17] op_sel_hi:[1,0]
	v_pk_mul_f32 v[52:53], v[52:53], v[16:17] op_sel_hi:[1,0]
	v_pk_mul_f32 v[50:51], v[50:51], v[16:17] op_sel_hi:[1,0]
	v_pk_mul_f32 v[48:49], v[48:49], v[16:17] op_sel_hi:[1,0]
	v_pk_mul_f32 v[46:47], v[46:47], v[16:17] op_sel_hi:[1,0]
	v_pk_mul_f32 v[44:45], v[44:45], v[16:17] op_sel_hi:[1,0]
	v_pk_mul_f32 v[42:43], v[42:43], v[16:17] op_sel_hi:[1,0]
	v_pk_mul_f32 v[40:41], v[40:41], v[16:17] op_sel_hi:[1,0]
	v_pk_mul_f32 v[38:39], v[38:39], v[16:17] op_sel_hi:[1,0]
	v_pk_mul_f32 v[36:37], v[36:37], v[16:17] op_sel_hi:[1,0]
	v_pk_mul_f32 v[34:35], v[34:35], v[16:17] op_sel_hi:[1,0]
; #define SWRITEO(boff, i) do { *(LAS bf16x8*)(lds + (boff) + kn_st) = skn[i]; *(LAS bf16x8*)(lds + (boff) + v_stw) = sv[i]; if (krw) *(LAS bf16x8*)(lds + (boff) + kr_st) = skr[i]; } while (0)
; #define PVO(boff) do { pv_one<0>(o0, vb0 + (boff), pa0, pa1, pa2, pa3); pv_one<1>(o1, vb0 + (boff), pa0, pa1, pa2, pa3); } while (0)
; #define SWAIT() asm volatile("s_waitcnt vmcnt(2)" ::: "memory")
; #define RESC(a) do { if (__any((a) < 1.f)) { _Pragma("unroll") for (int r = 0; r < 16; ++r) { o0[r] *= (a); o1[r] *= (a); } } } while (0)
; #define ROT() do { const int _t = bV; bV = bK; bK = bW; bW = _t; } while (0)
; template <bool FIRST> __device__ __forceinline__ void psm_apply(f32x16& p0, f32x16& p1, float pmax, float& m_reg, f32x16& negm, float& alpha) {
;     alpha = 1.f;
;     if (FIRST || !__builtin_expect(__all(pmax <= THR2), 1)) {
;         const float delta = FIRST ? pmax : fmaxf(pmax, 0.f);
;         if (!FIRST) alpha = __builtin_amdgcn_exp2f(-delta);
;         m_reg += delta;
; #pragma unroll
;         for (int r = 0; r < 16; ++r) { p0[r] -= delta; p1[r] -= delta; negm[r] = -m_reg; }
;     }
; #pragma unroll
;     for (int r = 0; r < 16; ++r) p0[r] = EXP_PROBE ? fmaf(p0[r], 0.001f, 1.f) : __builtin_amdgcn_exp2f(p0[r]);
; }
; template <int DQK, bool FIXM> ...
;     ...
;         if constexpr (FIXM) pv_psm<true>(o0, o1, vb0 + bV, pa0, pa1, pa2, pa3, pA0, pA1, m_reg, negm, alA); else { PVO(bV); partialSM<false>(pA0, pA1, m_reg, negm, alA); }
;         SWAIT(); SWRITEO(bW, 1);
;         if (!FIXM) RESC(alA); ROT();
;     }
.LBB0_540:
	v_add_f32_e32 v4, v228, v229
	v_fmac_f32_e32 v4, v227, v223
	v_add_f32_e32 v223, v126, v127
	s_add_i32 s35, s35, 2
	v_fmac_f32_e32 v223, v4, v2
	v_add_u32_e32 v226, 0x80, v226
	s_mov_b32 s37, s11
	s_cmp_ge_u32 s36, s12
	v_add_u32_e32 v225, 0x80, v225
	s_cbranch_scc1 .Lmla_exit
	s_mov_b32 s0, s13
	s_mov_b32 s13, s11
	s_mov_b32 s11, s10
	v_mov_b32_e32 v227, v16
	s_branch .LBB0_523
.Lmla_b_noload:
	s_waitcnt vmcnt(0)
	s_branch .Lmla_b_ld_done
.LBB0_542:
	v_max_f32_e32 v2, v2, v2
	v_max_f32_e32 v16, 0, v2
	v_exp_f32_e64 v2, -v16
	v_add_f32_e32 v224, v224, v16
	v_xor_b32_e32 v82, 0x80000000, v224
	v_pk_add_f32 v[130:131], v[130:131], v[16:17] op_sel_hi:[1,0] neg_lo:[0,1] neg_hi:[0,1]
	v_pk_add_f32 v[132:133], v[132:133], v[16:17] op_sel_hi:[1,0] neg_lo:[0,1] neg_hi:[0,1]
	v_pk_add_f32 v[134:135], v[134:135], v[16:17] op_sel_hi:[1,0] neg_lo:[0,1] neg_hi:[0,1]
	v_pk_add_f32 v[136:137], v[136:137], v[16:17] op_sel_hi:[1,0] neg_lo:[0,1] neg_hi:[0,1]
	v_pk_add_f32 v[138:139], v[138:139], v[16:17] op_sel_hi:[1,0] neg_lo:[0,1] neg_hi:[0,1]
	v_pk_add_f32 v[140:141], v[140:141], v[16:17] op_sel_hi:[1,0] neg_lo:[0,1] neg_hi:[0,1]
	v_pk_add_f32 v[142:143], v[142:143], v[16:17] op_sel_hi:[1,0] neg_lo:[0,1] neg_hi:[0,1]
	v_pk_add_f32 v[144:145], v[144:145], v[16:17] op_sel_hi:[1,0] neg_lo:[0,1] neg_hi:[0,1]
	v_sub_f32_e32 v129, v129, v16
	v_sub_f32_e32 v128, v128, v16
	v_sub_f32_e32 v127, v127, v16
	v_sub_f32_e32 v126, v126, v16
	v_sub_f32_e32 v125, v125, v16
	v_sub_f32_e32 v124, v124, v16
	v_sub_f32_e32 v123, v123, v16
	v_sub_f32_e32 v122, v122, v16
	v_sub_f32_e32 v121, v121, v16
	v_sub_f32_e32 v120, v120, v16
	v_sub_f32_e32 v119, v119, v16
	v_sub_f32_e32 v118, v118, v16
	v_sub_f32_e32 v117, v117, v16
	v_sub_f32_e32 v116, v116, v16
	v_sub_f32_e32 v115, v115, v16
	v_sub_f32_e32 v114, v114, v16
	v_mov_b32_e32 v83, v82
	v_mov_b32_e32 v84, v82
	v_mov_b32_e32 v85, v82
	v_mov_b32_e32 v86, v82
	v_mov_b32_e32 v87, v82
	v_mov_b32_e32 v88, v82
	v_mov_b32_e32 v89, v82
	v_mov_b32_e32 v90, v82
	v_mov_b32_e32 v91, v82
	v_mov_b32_e32 v92, v82
	v_mov_b32_e32 v93, v82
	v_mov_b32_e32 v94, v82
	v_mov_b32_e32 v95, v82
	v_mov_b32_e32 v96, v82
	v_mov_b32_e32 v97, v82
	s_branch .LBB0_527
.LBB0_543:
	v_max_f32_e32 v128, v128, v128
	v_max_f32_e32 v128, 0, v128
	v_exp_f32_e64 v16, -v128
	v_add_f32_e32 v224, v224, v128
	v_xor_b32_e32 v82, 0x80000000, v224
	v_pk_add_f32 v[130:131], v[130:131], v[128:129] op_sel_hi:[1,0] neg_lo:[0,1] neg_hi:[0,1]
	v_pk_add_f32 v[132:133], v[132:133], v[128:129] op_sel_hi:[1,0] neg_lo:[0,1] neg_hi:[0,1]
	v_pk_add_f32 v[134:135], v[134:135], v[128:129] op_sel_hi:[1,0] neg_lo:[0,1] neg_hi:[0,1]
	v_pk_add_f32 v[136:137], v[136:137], v[128:129] op_sel_hi:[1,0] neg_lo:[0,1] neg_hi:[0,1]
	v_pk_add_f32 v[138:139], v[138:139], v[128:129] op_sel_hi:[1,0] neg_lo:[0,1] neg_hi:[0,1]
	v_pk_add_f32 v[140:141], v[140:141], v[128:129] op_sel_hi:[1,0] neg_lo:[0,1] neg_hi:[0,1]
	v_pk_add_f32 v[142:143], v[142:143], v[128:129] op_sel_hi:[1,0] neg_lo:[0,1] neg_hi:[0,1]
	v_pk_add_f32 v[144:145], v[144:145], v[128:129] op_sel_hi:[1,0] neg_lo:[0,1] neg_hi:[0,1]
	v_sub_f32_e32 v113, v113, v128
	v_sub_f32_e32 v112, v112, v128
	v_sub_f32_e32 v111, v111, v128
	v_sub_f32_e32 v110, v110, v128
	v_sub_f32_e32 v109, v109, v128
	v_sub_f32_e32 v108, v108, v128
	v_sub_f32_e32 v107, v107, v128
	v_sub_f32_e32 v106, v106, v128
	v_sub_f32_e32 v105, v105, v128
	v_sub_f32_e32 v104, v104, v128
	v_sub_f32_e32 v103, v103, v128
	v_sub_f32_e32 v102, v102, v128
	v_sub_f32_e32 v101, v101, v128
	v_sub_f32_e32 v100, v100, v128
	v_sub_f32_e32 v99, v99, v128
	v_sub_f32_e32 v98, v98, v128
	v_mov_b32_e32 v83, v82
	v_mov_b32_e32 v84, v82
	v_mov_b32_e32 v85, v82
	v_mov_b32_e32 v86, v82
	v_mov_b32_e32 v87, v82
	v_mov_b32_e32 v88, v82
	v_mov_b32_e32 v89, v82
	v_mov_b32_e32 v90, v82
	v_mov_b32_e32 v91, v82
	v_mov_b32_e32 v92, v82
	v_mov_b32_e32 v93, v82
	v_mov_b32_e32 v94, v82
	v_mov_b32_e32 v95, v82
	v_mov_b32_e32 v96, v82
	v_mov_b32_e32 v97, v82
	s_branch .LBB0_536
.Lmla_exit:
	v_add_u32_e32 v17, s11, v213
	v_mov_b64_e32 v[66:67], v[82:83]
	v_mov_b64_e32 v[68:69], v[84:85]
	v_mov_b64_e32 v[70:71], v[86:87]
	v_mov_b64_e32 v[72:73], v[88:89]
	v_mov_b64_e32 v[74:75], v[90:91]
	v_mov_b64_e32 v[76:77], v[92:93]
	v_mov_b64_e32 v[78:79], v[94:95]
	v_mov_b64_e32 v[80:81], v[96:97]
	s_branch .LBB0_544

; __device__ __forceinline__ void xcd_barrier(const XcdBarrier& b) {
;     asm volatile("s_waitcnt vmcnt(0)" ::: "memory");
;     __syncthreads();
;     if (threadIdx.x == 0) {
;         unsigned* bar = b.bar;
;         __builtin_amdgcn_s_waitcnt(0);
;         unsigned nloc = b.st[0], nx = b.st[1];
;         if (nloc == 0u) { xcd_barrier_complete(bar, b.x, nloc, nx); b.st[0] = nloc; b.st[1] = nx; }
.LBB0_548:
	s_cmp_lg_u32 s99, 0
	s_cbranch_scc1 .Ltr_fw_0
	v_readlane_b32 s24, v254, 8
	v_readlane_b32 s27, v254, 11
	v_readlane_b32 s25, v254, 9
	v_readlane_b32 s26, v254, 10
	s_cmp_lt_i32 s27, 7
	s_mov_b32 s20, s72
	s_cbranch_scc1 .LBB0_598
	s_waitcnt vmcnt(0)
	v_cmp_eq_u32_e32 vcc, 0, v0
	s_barrier
	s_and_saveexec_b64 s[0:1], vcc
	s_cbranch_execz .LBB0_597
	s_add_i32 s2, 0, 0x24240
	v_mov_b32_e32 v1, s2
	s_waitcnt vmcnt(0) expcnt(0) lgkmcnt(0)
	ds_read_b32 v3, v1
	s_add_i32 s2, 0, 0x24244
	v_mov_b32_e32 v1, s2
	ds_read_b32 v1, v1
	s_waitcnt lgkmcnt(1)
	v_cmp_ne_u32_e32 vcc, 0, v3
	s_cbranch_vccnz .LBB0_565
	v_readlane_b32 s2, v254, 12
	v_readlane_b32 s3, v254, 13
	s_load_dwordx2 s[6:7], s[2:3], 0x4
	v_readlane_b32 s36, v254, 8
	v_readlane_b32 s37, v254, 9
	s_add_u32 s2, s36, 0x4200
	s_addc_u32 s3, s37, 0
	s_add_u32 s4, s36, 0x4400
	s_addc_u32 s5, s37, 0
	s_waitcnt lgkmcnt(0)
	s_mul_i32 s44, s6, s33
	s_add_u32 s6, s36, 0x4500
	s_mul_i32 s44, s44, s7
	s_addc_u32 s7, s37, 0
	s_add_u32 s8, s36, 0x4600
	s_addc_u32 s9, s37, 0
	s_add_u32 s10, s36, 0x4700
	s_addc_u32 s11, s37, 0
	s_add_u32 s12, s36, 0x4800
	s_addc_u32 s13, s37, 0
	s_add_u32 s14, s36, 0x4900
	s_addc_u32 s15, s37, 0
	s_add_u32 s16, s36, 0x4a00
	s_addc_u32 s17, s37, 0
	s_add_u32 s18, s36, 0x4b00
	s_addc_u32 s19, s37, 0
	s_add_u32 s20, s36, 0x4c00
	s_addc_u32 s21, s37, 0
	s_add_u32 s22, s36, 0x4d00
	s_addc_u32 s23, s37, 0
	s_add_u32 s24, s36, 0x4e00
	s_addc_u32 s25, s37, 0
	s_add_u32 s26, s36, 0x4f00
	s_addc_u32 s27, s37, 0
	s_add_u32 s28, s36, 0x5000
	s_addc_u32 s29, s37, 0
	s_add_u32 s30, s36, 0x5100
	s_addc_u32 s31, s37, 0
	s_add_u32 s34, s36, 0x5200
	s_addc_u32 s35, s37, 0
	s_add_u32 s36, s36, 0x5300
	s_addc_u32 s37, s37, 0
	s_mov_b32 s45, 1
	v_mov_b32_e32 v17, 0
	v_readlane_b32 s38, v254, 10
	v_readlane_b32 s39, v254, 11
	s_branch .LBB0_553

; __device__ __forceinline__ int chunk_lo(int gw, int M, int NGW) { return (int)(((long)gw * M) / NGW); }
; __device__ __forceinline__ void ffn_norm_route_phase(Frame& F, int l) {
;     ...
;     const int r0 = 2 * chunk_lo(F.gw, M >> 1, F.NGW), r1 = 2 * chunk_lo(F.gw + 1, M >> 1, F.NGW);
;     RowVec V; RowRaw curA, curB, nxtA, nxtB; int vcur = -1;
;     if (r0 < r1) { load_rowraw_b(nxtA, X + (size_t)r0 * 1024, nullptr, F.lane); load_rowraw_b(nxtB, X + (size_t)(r0 + 1) * 1024, nullptr, F.lane); }
;     float keep[36];
; #pragma unroll
;     for (int o = 0; o < 36; ++o) keep[o] = 0.f;
;     int pit = 0;
;     for (int m = r0; m < r1; m += 2, ++pit) {
.LBB0_702:
	s_lshl_b32 s16, s0, 1
	s_lshl_b32 s7, s6, 1
	s_cmp_le_i32 s7, s16
	s_cbranch_scc0 .LBB0_704
	v_and_b32_e32 v2, 31, v34
	s_mov_b64 s[0:1], 0
	s_branch .LBB0_705
.Ltr_fw_0:
	s_branch .Ltr_fw_1
.Ltr_bw_0:
	s_branch .Latt_shared
.LBB0_704:
	s_mov_b64 s[0:1], -1

; __device__ __forceinline__ int chunk_lo(int gw, int M, int NGW) { return (int)(((long)gw * M) / NGW); }
; __device__ __forceinline__ void ffn_norm_route_phase(Frame& F, int l) {
;     ...
;     const int r0 = 2 * chunk_lo(F.gw, M >> 1, F.NGW), r1 = 2 * chunk_lo(F.gw + 1, M >> 1, F.NGW);
;     RowVec V; RowRaw curA, curB, nxtA, nxtB; int vcur = -1;
;     if (r0 < r1) { load_rowraw_b(nxtA, X + (size_t)r0 * 1024, nullptr, F.lane); load_rowraw_b(nxtB, X + (size_t)(r0 + 1) * 1024, nullptr, F.lane); }
;     float keep[36];
; #pragma unroll
;     for (int o = 0; o < 36; ++o) keep[o] = 0.f;
;     int pit = 0;
;     for (int m = r0; m < r1; m += 2, ++pit) {
.LBB0_1100:
	s_and_b32 s31, s0, -2
	s_cmp_lg_u32 s0, s31
	s_cselect_b64 s[0:1], -1, 0
	s_and_b64 vcc, exec, s[0:1]
	s_cbranch_vccnz .LBB0_1102
	s_branch .LBB0_1104
.Ltr_fw_1:
	s_branch .Ltr_fw_2
.Ltr_bw_1:
	s_branch .Ltr_bw_0
.LBB0_1101:
	s_mov_b32 s31, 0
	s_cbranch_execz .LBB0_1104

; __device__ __forceinline__ int chunk_lo(int gw, int M, int NGW) { return (int)(((long)gw * M) / NGW); }
; __device__ __forceinline__ void ffn_norm_route_phase(Frame& F, int l) {
;     ...
;     const int r0 = 2 * chunk_lo(F.gw, M >> 1, F.NGW), r1 = 2 * chunk_lo(F.gw + 1, M >> 1, F.NGW);
;     RowVec V; RowRaw curA, curB, nxtA, nxtB; int vcur = -1;
;     if (r0 < r1) { load_rowraw_b(nxtA, X + (size_t)r0 * 1024, nullptr, F.lane); load_rowraw_b(nxtB, X + (size_t)(r0 + 1) * 1024, nullptr, F.lane); }
;     float keep[36];
; #pragma unroll
;     for (int o = 0; o < 36; ++o) keep[o] = 0.f;
;     int pit = 0;
;     for (int m = r0; m < r1; m += 2, ++pit) {
.LBB0_1573:
	s_and_b32 s31, s0, -2
	s_cmp_lg_u32 s0, s31
	s_cselect_b64 s[0:1], -1, 0
	s_and_b64 vcc, exec, s[0:1]
	s_cbranch_vccnz .LBB0_1575
	s_branch .LBB0_1577
.Ltr_fw_2:
	s_branch .Ltr_fw_3
.Ltr_bw_2:
	s_branch .Ltr_bw_1
.LBB0_1574:
	s_mov_b32 s31, 0
	s_cbranch_execz .LBB0_1577

; #define PG8_WAIT_V(n) asm volatile("s_waitcnt vmcnt(" #n ")" ::: "memory")
; #define PG8_BAR __builtin_amdgcn_s_barrier()
; template <class Epi, class Sched, bool ALIGN_EPI = false>
; __device__ __forceinline__ void gemm_phase(LAS unsigned char* lds, const Gemm g, const Sched& S, const Epi& E, const int tid) {
;     ...
;         if constexpr (ALIGN_EPI) { if (wr == 0) PG8_BAR; }
;         E(acc, cur, wr, wc, fr, fq);
;         if (!has_next) break;
; #pragma unroll
;         for (int a = 0; a < 2; ++a)
; #pragma unroll
;             for (int b = 0; b < 2; ++b)
; #pragma unroll
;                 for (int m = 0; m < 4; ++m)
; #pragma unroll
;                     for (int n = 0; n < 2; ++n) acc[a][b][m][n] = (f32x4){0.f, 0.f, 0.f, 0.f};
;         cur = nxt; cA = nA; cB = nB; ++ui;
;         if constexpr (GA) { _Pragma("unroll") for (int _h = 0; _h < 2; ++_h) _Pragma("unroll") for (int _i = 0; _i < 2; ++_i) ra[_h][_i] = rn[_h][_i]; }
;         if constexpr (ALIGN_EPI) { if (wr == 1) PG8_BAR; }
;     }
;     PG8_WAIT_V(0);
;     if constexpr (!ALIGN_EPI) { if (wr == 0) PG8_BAR; }
;     PG8_BAR;
.LBB0_1854:
	s_andn2_b64 vcc, exec, s[6:7]
	s_cbranch_vccnz .LBB0_1841
	s_barrier
	s_branch .LBB0_1841
.Ltr_fw_3:
	s_branch .Ltr_fw_4
.Ltr_bw_3:
	s_branch .Ltr_bw_2
.LBB0_1856:
	s_waitcnt vmcnt(0)
	s_mov_b32 s20, s88
	s_barrier

; __device__ __forceinline__ int chunk_lo(int gw, int M, int NGW) { return (int)(((long)gw * M) / NGW); }
; __device__ __forceinline__ void ffn_norm_route_phase(Frame& F, int l) {
;     ...
;     const int r0 = 2 * chunk_lo(F.gw, M >> 1, F.NGW), r1 = 2 * chunk_lo(F.gw + 1, M >> 1, F.NGW);
;     RowVec V; RowRaw curA, curB, nxtA, nxtB; int vcur = -1;
;     if (r0 < r1) { load_rowraw_b(nxtA, X + (size_t)r0 * 1024, nullptr, F.lane); load_rowraw_b(nxtB, X + (size_t)(r0 + 1) * 1024, nullptr, F.lane); }
;     float keep[36];
; #pragma unroll
;     for (int o = 0; o < 36; ++o) keep[o] = 0.f;
;     int pit = 0;
;     for (int m = r0; m < r1; m += 2, ++pit) {
.LBB0_2131:
	s_lshl_b32 s16, s0, 1
	s_lshl_b32 s9, s6, 1
	s_cmp_le_i32 s9, s16
	s_cbranch_scc0 .LBB0_2133
	v_and_b32_e32 v2, 31, v34
	s_mov_b64 s[0:1], 0
	s_branch .LBB0_2134
.Ltr_fw_4:
	s_branch .Ltr_fw_5
.Ltr_bw_4:
	s_branch .Ltr_bw_3
.LBB0_2133:
	s_mov_b64 s[0:1], -1

; __device__ __forceinline__ int chunk_lo(int gw, int M, int NGW) { return (int)(((long)gw * M) / NGW); }
; __device__ __forceinline__ void ffn_norm_route_phase(Frame& F, int l) {
;     ...
;     const int r0 = 2 * chunk_lo(F.gw, M >> 1, F.NGW), r1 = 2 * chunk_lo(F.gw + 1, M >> 1, F.NGW);
;     RowVec V; RowRaw curA, curB, nxtA, nxtB; int vcur = -1;
;     if (r0 < r1) { load_rowraw_b(nxtA, X + (size_t)r0 * 1024, nullptr, F.lane); load_rowraw_b(nxtB, X + (size_t)(r0 + 1) * 1024, nullptr, F.lane); }
;     float keep[36];
; #pragma unroll
;     for (int o = 0; o < 36; ++o) keep[o] = 0.f;
;     int pit = 0;
;     for (int m = r0; m < r1; m += 2, ++pit) {
.LBB0_2553:
	s_and_b32 s35, s0, -2
	s_cmp_lg_u32 s0, s35
	s_cselect_b64 s[0:1], -1, 0
	s_and_b64 vcc, exec, s[0:1]
	s_cbranch_vccnz .LBB0_2555
	s_branch .LBB0_2557
.Ltr_fw_5:
	s_branch .Ltr_fw_6
.Ltr_bw_5:
	s_branch .Ltr_bw_4
.LBB0_2554:
	s_mov_b32 s35, 0
	s_cbranch_execz .LBB0_2557

; __device__ __forceinline__ int chunk_lo(int gw, int M, int NGW) { return (int)(((long)gw * M) / NGW); }
; __device__ __forceinline__ void ffn_norm_route_phase(Frame& F, int l) {
;     ...
;     const int r0 = 2 * chunk_lo(F.gw, M >> 1, F.NGW), r1 = 2 * chunk_lo(F.gw + 1, M >> 1, F.NGW);
;     RowVec V; RowRaw curA, curB, nxtA, nxtB; int vcur = -1;
;     if (r0 < r1) { load_rowraw_b(nxtA, X + (size_t)r0 * 1024, nullptr, F.lane); load_rowraw_b(nxtB, X + (size_t)(r0 + 1) * 1024, nullptr, F.lane); }
;     float keep[36];
; #pragma unroll
;     for (int o = 0; o < 36; ++o) keep[o] = 0.f;
;     int pit = 0;
;     for (int m = r0; m < r1; m += 2, ++pit) {
.LBB0_3026:
	s_and_b32 s35, s0, -2
	s_cmp_lg_u32 s0, s35
	s_cselect_b64 s[0:1], -1, 0
	s_and_b64 vcc, exec, s[0:1]
	s_cbranch_vccnz .LBB0_3028
	s_branch .LBB0_3030
.Ltr_fw_6:
	s_branch .Ltr_fw_7
.Ltr_bw_6:
	s_branch .Ltr_bw_5
.LBB0_3027:
	s_mov_b32 s35, 0
	s_cbranch_execz .LBB0_3030

; __device__ __forceinline__ unsigned cvt_pk_bf16(float lo, float hi) { unsigned r; asm volatile("v_cvt_pk_bf16_f32 %0, %1, %2" : "=v"(r) : "v"(lo), "v"(hi)); return r; }
; __device__ __forceinline__ void ab_prep_phase(Frame& F, int li) {
;     const bf16_t* P = (const bf16_t*)(F.ws + R_P);
;     bf16_t* CQN = (bf16_t*)(F.ws + R_CQN); bf16_t* CKVN = (bf16_t*)(F.ws + R_CKVN); bf16_t* KR = (bf16_t*)(F.ws + R_KR);
;     bf16_t* QB = (bf16_t*)(F.ws + R_QB); bf16_t* KB = (bf16_t*)(F.ws + R_KB); bf16_t* VB = (bf16_t*)(F.ws + R_VB);
;     const f32x2* rope = (const f32x2*)(F.ws + WS_ROPE);
;     const float* qn = F.in[11] + li * QLORA; const float* kvn = F.in[13] + li * KVLORA; const float* gqn = F.in[15] + li * 64; const float* gkn = F.in[16] + li * 64;
;     const int l = F.lane;
;     for (int m = F.gw; m < MROWS; m += F.NGW) {
;         const bf16_t* p = P + (size_t)m * AB_INP;
;         const bool lat = m < NLAT; const int t = m & (SEQ - 1), gr = t >> 6, gc = t & 63;
;         const unsigned* pc = (const unsigned*)(p + 6 * l); const unsigned c0 = pc[0], c1 = pc[1], c2 = pc[2];
;         const u32x2 kv = *(const u32x2*)(p + 384 + 4 * l);
;         const unsigned krw = *(const unsigned*)(p + 640 + 2 * (l & 15));
;         const u32x4 gq = *(const u32x4*)(p + 672 + 8 * l);
;         const unsigned gkw = *(const unsigned*)(p + 1184 + 2 * l), gvw = *(const unsigned*)(p + 1312 + 2 * l);
;     ...
;         if (l < 16) { float x1 = bf16lo(krw), x2 = bf16hi(krw);
;             if (lat) { const f32x2 cs = (l < 8) ? rope[gr * 8 + l] : rope[2048 + gc * 8 + (l - 8)]; const float a = x1 * cs.x - x2 * cs.y, b = x1 * cs.y + x2 * cs.x; x1 = a; x2 = b; }
;             *(unsigned*)(KR + (size_t)m * 32 + 2 * l) = cvt_pk_bf16(x1, x2); }
.LBB0_3343:
	s_ashr_i32 s2, s2, 6
	s_lshl_b32 s3, s3, 3
	s_add_i32 s14, s3, s2
	s_cmp_gt_i32 s14, 0x81ff
	s_cbranch_scc1 .LBB0_3364
	v_readlane_b32 s36, v254, 33
	v_and_b32_e32 v1, 63, v2
	v_mov_b32_e32 v15, 0
	v_readlane_b32 s46, v254, 43
	v_readlane_b32 s47, v254, 44
	v_lshlrev_b32_e32 v4, 4, v1
	v_mov_b32_e32 v5, v15
	s_mov_b64 s[22:23], s[46:47]
	v_readlane_b32 s37, v254, 34
	v_readlane_b32 s38, v254, 35
	v_readlane_b32 s39, v254, 36
	v_readlane_b32 s40, v254, 37
	v_readlane_b32 s41, v254, 38
	v_readlane_b32 s42, v254, 39
	v_readlane_b32 s43, v254, 40
	v_readlane_b32 s44, v254, 41
	v_readlane_b32 s45, v254, 42
	v_readlane_b32 s48, v254, 45
	v_readlane_b32 s49, v254, 46
	v_readlane_b32 s50, v254, 47
	v_readlane_b32 s51, v254, 48
	v_lshl_add_u64 v[16:17], s[22:23], 0, v[4:5]
	v_and_b32_e32 v5, 7, v2
	s_add_u32 s16, s0, 0x180000
	s_mov_b64 s[18:19], s[42:43]
	s_mov_b64 s[26:27], s[50:51]
	v_lshlrev_b32_e32 v6, 5, v5
	v_mov_b32_e32 v7, v15
	v_and_b32_e32 v61, 31, v2
	v_readlane_b32 s36, v254, 49
	s_addc_u32 s17, s1, 0
	v_mul_u32_u24_e32 v3, 6, v1
	v_lshl_add_u64 v[18:19], s[26:27], 0, v[6:7]
	v_lshl_add_u64 v[20:21], s[0:1], 0, v[6:7]
	v_lshlrev_b32_e32 v6, 3, v61
	v_readlane_b32 s37, v254, 50
	s_ashr_i32 s15, s14, 31
	v_lshlrev_b32_e32 v14, 2, v1
	v_lshl_add_u64 v[24:25], s[36:37], 0, v[6:7]
	v_lshlrev_b32_e32 v6, 2, v3
	s_lshl_b64 s[10:11], s[14:15], 6
	v_lshl_add_u64 v[26:27], s[18:19], 0, v[6:7]
	v_lshl_add_u64 v[6:7], s[10:11], 0, v[14:15]
	s_mov_b64 s[10:11], 0x1ea00000
	v_lshl_add_u64 v[28:29], v[6:7], 0, s[10:11]
	s_lshl_b64 s[10:11], s[14:15], 8
	v_or_b32_e32 v30, s10, v14
	v_mov_b32_e32 v31, s11
	s_lshl_b64 s[10:11], s[14:15], 10
	v_or_b32_e32 v6, s10, v4
	v_mov_b32_e32 v7, s11
	s_mov_b64 s[10:11], 0x1ed00000
	v_lshlrev_b32_e32 v8, 3, v1
	v_lshl_add_u64 v[32:33], v[6:7], 0, s[10:11]
	s_lshl_b64 s[10:11], s[14:15], 9
	v_or_b32_e32 v6, s10, v8
	v_mov_b32_e32 v7, s11
	s_mov_b64 s[10:11], 0x16700000
	v_lshl_add_u64 v[34:35], v[6:7], 0, s[10:11]
	v_lshlrev_b32_e32 v6, 1, v3
	v_mov_b32_e32 v7, v15
	v_mov_b32_e32 v3, 0x300
	v_mad_i64_i32 v[36:37], s[10:11], s14, v3, v[6:7]
	s_mul_hi_i32 s10, s14, 0xc00
	s_mul_i32 s12, s14, 0xc00
	v_cmp_lt_u32_e64 s[6:7], 3, v5
	v_mov_b32_e32 v39, s10
	v_or_b32_e32 v4, s12, v4
	v_mov_b32_e32 v5, s10
	s_mov_b64 s[10:11], 0xec00540
	v_and_b32_e32 v2, 15, v2
	v_lshl_add_u64 v[40:41], v[4:5], 0, s[10:11]
	v_lshl_or_b32 v2, v2, 2, s12
	v_mov_b32_e32 v3, v39
	s_mov_b64 s[10:11], 0xec00500
	v_lshl_add_u64 v[42:43], v[2:3], 0, s[10:11]
	v_or_b32_e32 v2, s12, v8
	s_mov_b64 s[10:11], 0xec00300
	s_ashr_i32 s21, s20, 31
	v_lshl_add_u64 v[44:45], v[2:3], 0, s[10:11]
	v_mov_b32_e32 v2, 0xc00
	s_mov_b64 s[8:9], 0x185000
	v_readlane_b32 s38, v254, 51
	v_readlane_b32 s39, v254, 52
	v_readlane_b32 s44, v254, 57
	s_mov_b64 s[28:29], s[20:21]
	v_mad_i64_i32 v[46:47], s[10:11], s14, v2, v[6:7]
	v_mbcnt_lo_u32_b32 v2, -1, 0
	v_cmp_gt_u32_e64 s[2:3], 16, v1
	v_cmp_gt_u32_e64 s[4:5], 8, v1
	v_add_u32_e32 v60, 0x7f8, v1
	v_lshl_add_u64 v[22:23], v[20:21], 0, s[8:9]
	v_cmp_lt_u32_e64 s[8:9], 15, v61
	v_or_b32_e32 v62, 0xa00, v61
	s_lshl_b64 s[18:19], s[20:21], 6
	s_lshl_b64 s[20:21], s[20:21], 8
	s_lshl_b64 s[22:23], s[28:29], 10
	s_lshl_b64 s[24:25], s[28:29], 9
	s_mul_hi_i32 s27, s28, 0x300
	s_mul_i32 s26, s28, 0x300
	v_or_b32_e32 v38, s12, v14
	s_mul_hi_i32 s29, s28, 0xc00
	s_mov_b32 s44, s28
	s_mulk_i32 s28, 0xc00
	s_mov_b32 s15, 0xec00000
	s_mov_b32 s31, 0
	v_mov_b32_e32 v63, 0x358637bd
	s_mov_b32 s38, 0x800000
	s_mov_b32 s39, 0x14e00000
	s_mov_b64 s[34:35], 0x18cf80
	s_mov_b64 s[36:37], 0xcf80
	v_mbcnt_hi_u32_b32 v64, -1, v2
	v_readlane_b32 s40, v254, 53
	v_readlane_b32 s41, v254, 54
	v_readlane_b32 s42, v254, 55
	v_readlane_b32 s43, v254, 56
	v_readlane_b32 s45, v254, 58
	v_readlane_b32 s46, v254, 59
	v_readlane_b32 s47, v254, 60
	v_readlane_b32 s48, v254, 61
	v_readlane_b32 s49, v254, 62
	v_readlane_b32 s50, v254, 63
	v_readlane_b32 s51, v255, 0
	s_branch .LBB0_3347
.Ltr_fw_7:
	s_branch .LBB0_3575
.Ltr_bw_7:
	s_branch .Ltr_bw_6
.LBB0_3345:
	s_or_b64 exec, exec, s[10:11]
	global_load_dwordx2 v[4:5], v[4:5], off
	s_waitcnt vmcnt(0)
	v_pk_mul_f32 v[8:9], v[2:3], v[4:5] op_sel:[1,1] op_sel_hi:[1,0]
	v_pk_mul_f32 v[6:7], v[2:3], v[4:5]
	v_pk_fma_f32 v[2:3], v[2:3], v[4:5], v[8:9] op_sel_hi:[0,1,1]
	v_sub_f32_e32 v2, v6, v8

; __device__ __forceinline__ void attn_phase(Frame& F, int li) {
;     ...
;     float mfixB; { float gq = 0.f, gk = 0.f; const float* a = F.in[15] + li * 64; const float* b = F.in[16] + li * 64;
;         for (int i = 0; i < 64; ++i) { gq = fmaxf(gq, fabsf(a[i])); gk = fmaxf(gk, fabsf(b[i])); } mfixB = 64.f * gq * gk * SC_B * 1.02f; }
.LBB0_3513:
	s_add_u32 s4, s18, s2
	s_addc_u32 s5, s19, s3
	global_load_dwordx4 v[8:11], v1, s[4:5] offset:272
	global_load_dwordx4 v[12:15], v1, s[4:5] offset:256
	s_add_u32 s4, s16, s2
	s_addc_u32 s5, s17, s3
	global_load_dwordx4 v[16:19], v1, s[4:5] offset:256
	global_load_dwordx4 v[20:23], v1, s[4:5] offset:272
	s_add_u32 s2, s2, 32
	s_addc_u32 s3, s3, 0
	s_cmpk_eq_i32 s2, 0x100
	s_waitcnt vmcnt(0)
	v_max3_f32 v2, v5, |v12|, |v13|
	v_max3_f32 v2, v2, |v14|, |v15|
	v_max3_f32 v3, v6, |v16|, |v17|
	v_max3_f32 v2, v2, |v8|, |v9|
	v_max3_f32 v3, v3, |v18|, |v19|
	v_max3_f32 v5, v2, |v10|, |v11|
	v_max3_f32 v2, v3, |v20|, |v21|
	v_max3_f32 v6, v2, |v22|, |v23|
	s_cbranch_scc0 .LBB0_3513
	s_mov_b32 s99, 1
	s_branch .Ltr_bw_7

; __global__ void __launch_bounds__(NTHREADS, 2) fwd(Args args) {
	.amdhsa_kernel _Z3fwd4Args
		.amdhsa_group_segment_fixed_size 0
		.amdhsa_private_segment_fixed_size 0
		.amdhsa_kernarg_size 496
		.amdhsa_user_sgpr_count 2
		.amdhsa_user_sgpr_dispatch_ptr 0
		.amdhsa_user_sgpr_queue_ptr 0
		.amdhsa_user_sgpr_kernarg_segment_ptr 1
		.amdhsa_user_sgpr_dispatch_id 0
		.amdhsa_user_sgpr_kernarg_preload_length 0
		.amdhsa_user_sgpr_kernarg_preload_offset 0
		.amdhsa_user_sgpr_private_segment_size 0
		.amdhsa_uses_dynamic_stack 0
		.amdhsa_enable_private_segment 0
		.amdhsa_system_sgpr_workgroup_id_x 1
		.amdhsa_system_sgpr_workgroup_id_y 0
		.amdhsa_system_sgpr_workgroup_id_z 0
		.amdhsa_system_sgpr_workgroup_info 0
		.amdhsa_system_vgpr_workitem_id 0
		.amdhsa_next_free_vgpr 256
		.amdhsa_next_free_sgpr 102
		.amdhsa_accum_offset 256
		.amdhsa_reserve_vcc 1
		.amdhsa_float_round_mode_32 0
		.amdhsa_float_round_mode_16_64 0
		.amdhsa_float_denorm_mode_32 3
		.amdhsa_float_denorm_mode_16_64 3
		.amdhsa_dx10_clamp 1
		.amdhsa_ieee_mode 1
		.amdhsa_fp16_overflow 0
		.amdhsa_tg_split 0
		.amdhsa_exception_fp_ieee_invalid_op 0
		.amdhsa_exception_fp_denorm_src 0
		.amdhsa_exception_fp_ieee_div_zero 0
		.amdhsa_exception_fp_ieee_overflow 0
		.amdhsa_exception_fp_ieee_underflow 0
		.amdhsa_exception_fp_ieee_inexact 0
		.amdhsa_exception_int_div_zero 0
	.end_amdhsa_kernel

; __global__ void __launch_bounds__(NTHREADS, 2) fwd(Args args) {
amdhsa.kernels:
  - .agpr_count:     0
    .args:
      - .offset:         0
        .size:           240
        .value_kind:     by_value
      - .offset:         240
        .size:           4
        .value_kind:     hidden_block_count_x
      - .offset:         244
        .size:           4
        .value_kind:     hidden_block_count_y
      - .offset:         248
        .size:           4
        .value_kind:     hidden_block_count_z
      - .offset:         252
        .size:           2
        .value_kind:     hidden_group_size_x
      - .offset:         254
        .size:           2
        .value_kind:     hidden_group_size_y
      - .offset:         256
        .size:           2
        .value_kind:     hidden_group_size_z
      - .offset:         258
        .size:           2
        .value_kind:     hidden_remainder_x
      - .offset:         260
        .size:           2
        .value_kind:     hidden_remainder_y
      - .offset:         262
        .size:           2
        .value_kind:     hidden_remainder_z
      - .offset:         280
        .size:           8
        .value_kind:     hidden_global_offset_x
      - .offset:         288
        .size:           8
        .value_kind:     hidden_global_offset_y
      - .offset:         296
        .size:           8
        .value_kind:     hidden_global_offset_z
      - .offset:         304
        .size:           2
        .value_kind:     hidden_grid_dims
      - .offset:         360
        .size:           4
        .value_kind:     hidden_dynamic_lds_size
    .group_segment_fixed_size: 0
    .kernarg_segment_align: 8
    .kernarg_segment_size: 496
    .language:       OpenCL C
    .language_version:
      - 2
      - 0
    .max_flat_workgroup_size: 512
    .name:           _Z3fwd4Args
    .private_segment_fixed_size: 0
    .sgpr_count:     108
    .sgpr_spill_count: 71
    .symbol:         _Z3fwd4Args.kd
    .uniform_work_group_size: 1
    .uses_dynamic_stack: false
    .vgpr_count:     256
    .vgpr_spill_count: 0
    .wavefront_size: 64
